# peersel final stage: one 16-byte load of the lane's 16 candidate codes + v_bfe instead of 14 serial byte loads with vmcnt(0) waits
# speedup vs baseline: 1.0028x; 1.0028x over previous
; DI unsigned ordkey(float f) { const unsigned u = __float_as_uint(f); return (u & 0x80000000u) ? ~u : (u | 0x80000000u); }
; #define CE_DESC(x, y) do { const unsigned mx_ = (x) > (y) ? (x) : (y); const unsigned mn_ = (x) > (y) ? (y) : (x); (x) = mx_; (y) = mn_; } while (0)
; DI void sort16_desc(unsigned (&a)[16]) {
; #pragma unroll
;   for (int k = 2; k <= 16; k <<= 1)
; #pragma unroll
;     for (int j = k >> 1; j > 0; j >>= 1)
; #pragma unroll
;       for (int i = 0; i < 16; ++i) {
;         const int l = i ^ j;
;         if (l > i) { if ((i & k) == 0) CE_DESC(a[i], a[l]); else CE_DESC(a[l], a[i]); }
;       }
; }
; DI void peer_select_unit(const Params& p, int unit, char* lds, const bf16x8 (&kb)[4][4]) {
;     ...
;   for (int pass = 0; pass < 2; ++pass) {
;     const int rr = pass * 32 + (tid >> 3), part = tid & 7;
;     unsigned a[16], bq[16];
;     const float* srow = sc + rr * 132 + 16 * part;
; #pragma unroll
;     for (int j = 0; j < 4; ++j) {
;       const f32x4 v = *(const f32x4*)(srow + 4 * j);
; #pragma unroll
;       for (int e = 0; e < 4; ++e) a[4 * j + e] = (ordkey(v[e]) & ~127u) | (unsigned)(127 - (16 * part + 4 * j + e));
;     }
;     sort16_desc(a);
.LBB0_1653:
	v_add_u32_e32 v71, s69, v64
	v_mul_lo_u32 v76, v71, s2
	v_add_u32_e32 v77, v68, v76
	ds_read_b128 v[78:81], v77
	ds_read_b128 v[82:85], v77 offset:16
	ds_read_b128 v[86:89], v77 offset:32
	ds_read_b128 v[90:93], v77 offset:48
	v_cndmask_b32_e64 v70, 0, 1, s[20:21]
	s_waitcnt lgkmcnt(3)
	v_not_b32_e32 v77, v78
	v_or_b32_e32 v94, 0x80000000, v78
	v_not_b32_e32 v95, v79
	v_or_b32_e32 v96, 0x80000000, v79
	v_cmp_gt_i32_e32 vcc, 0, v79
	v_not_b32_e32 v79, v80
	v_or_b32_e32 v97, 0x80000000, v80
	v_cmp_gt_i32_e64 s[20:21], 0, v80
	v_not_b32_e32 v80, v81
	v_or_b32_e32 v98, 0x80000000, v81
	v_cmp_gt_i32_e64 s[22:23], 0, v81
	s_waitcnt lgkmcnt(2)
	v_not_b32_e32 v81, v82
	v_or_b32_e32 v99, 0x80000000, v82
	v_cmp_gt_i32_e64 s[24:25], 0, v82
	v_not_b32_e32 v82, v83
	v_or_b32_e32 v100, 0x80000000, v83
	v_cmp_gt_i32_e64 s[26:27], 0, v83
	v_not_b32_e32 v83, v84
	v_or_b32_e32 v101, 0x80000000, v84
	v_cmp_gt_i32_e64 s[28:29], 0, v84
	v_not_b32_e32 v84, v85
	v_or_b32_e32 v102, 0x80000000, v85
	v_cmp_gt_i32_e64 s[30:31], 0, v85
	s_waitcnt lgkmcnt(1)
	v_not_b32_e32 v85, v86
	v_or_b32_e32 v103, 0x80000000, v86
	v_cmp_gt_i32_e64 s[34:35], 0, v86
	v_not_b32_e32 v86, v87
	v_or_b32_e32 v104, 0x80000000, v87
	v_cmp_gt_i32_e64 s[36:37], 0, v87
	v_not_b32_e32 v87, v88
	v_or_b32_e32 v105, 0x80000000, v88
	v_cmp_gt_i32_e64 s[38:39], 0, v88
	v_not_b32_e32 v88, v89
	v_or_b32_e32 v106, 0x80000000, v89
	v_cmp_gt_i32_e64 s[40:41], 0, v89
	s_waitcnt lgkmcnt(0)
	v_not_b32_e32 v89, v90
	v_or_b32_e32 v107, 0x80000000, v90
	v_cmp_gt_i32_e64 s[42:43], 0, v90
	v_not_b32_e32 v90, v91
	v_or_b32_e32 v108, 0x80000000, v91
	v_cmp_gt_i32_e64 s[44:45], 0, v91
	v_not_b32_e32 v91, v92
	v_or_b32_e32 v109, 0x80000000, v92
	v_cmp_gt_i32_e64 s[46:47], 0, v92
	v_not_b32_e32 v92, v93
	v_or_b32_e32 v110, 0x80000000, v93
	v_cmp_gt_i32_e64 s[48:49], 0, v93
	v_cmp_gt_i32_e64 s[50:51], 0, v78
	v_cndmask_b32_e32 v78, v96, v95, vcc
	v_cndmask_b32_e64 v79, v97, v79, s[20:21]
	v_cndmask_b32_e64 v77, v94, v77, s[50:51]
	v_cndmask_b32_e64 v80, v98, v80, s[22:23]
	v_cndmask_b32_e64 v81, v99, v81, s[24:25]
	v_cndmask_b32_e64 v82, v100, v82, s[26:27]
	v_cndmask_b32_e64 v83, v101, v83, s[28:29]
	v_cndmask_b32_e64 v84, v102, v84, s[30:31]
	v_cndmask_b32_e64 v85, v103, v85, s[34:35]
	v_cndmask_b32_e64 v86, v104, v86, s[36:37]
	v_cndmask_b32_e64 v87, v105, v87, s[38:39]
	v_cndmask_b32_e64 v88, v106, v88, s[40:41]
	v_cndmask_b32_e64 v89, v107, v89, s[42:43]
	v_cndmask_b32_e64 v90, v108, v90, s[44:45]
	v_cndmask_b32_e64 v91, v109, v91, s[46:47]
	v_cndmask_b32_e64 v92, v110, v92, s[48:49]
	v_and_b32_e32 v77, 0xffffff80, v77
	v_and_b32_e32 v78, 0xffffff80, v78
	v_and_b32_e32 v79, 0xffffff80, v79
	v_and_b32_e32 v80, 0xffffff80, v80
	v_and_b32_e32 v81, 0xffffff80, v81
	v_and_b32_e32 v82, 0xffffff80, v82
	v_and_b32_e32 v83, 0xffffff80, v83
	v_and_b32_e32 v84, 0xffffff80, v84
	v_and_b32_e32 v85, 0xffffff80, v85
	v_and_b32_e32 v86, 0xffffff80, v86
	v_and_b32_e32 v87, 0xffffff80, v87
	v_and_b32_e32 v88, 0xffffff80, v88
	v_and_b32_e32 v89, 0xffffff80, v89
	v_and_b32_e32 v90, 0xffffff80, v90
	v_and_b32_e32 v91, 0xffffff80, v91
	v_and_b32_e32 v92, 0xffffff80, v92
	v_sub_u32_e32 v77, v77, v67
	v_sub_u32_e32 v78, v78, v67
	v_sub_u32_e32 v79, v79, v67
	v_sub_u32_e32 v80, v80, v67
	v_sub_u32_e32 v81, v81, v67
	v_sub_u32_e32 v82, v82, v67
	v_sub_u32_e32 v83, v83, v67
	v_sub_u32_e32 v84, v84, v67
	v_sub_u32_e32 v85, v85, v67
	v_sub_u32_e32 v86, v86, v67
	v_sub_u32_e32 v87, v87, v67
	v_sub_u32_e32 v88, v88, v67
	v_sub_u32_e32 v89, v89, v67
	v_sub_u32_e32 v90, v90, v67
	v_sub_u32_e32 v91, v91, v67
	v_sub_u32_e32 v92, v92, v67
	v_add_u32_e32 v77, 0x7f, v77
	v_add_u32_e32 v78, 0x7e, v78
	v_add_u32_e32 v79, 0x7d, v79
	v_add_u32_e32 v80, 0x7c, v80
	v_add_u32_e32 v81, 0x7b, v81
	v_add_u32_e32 v82, 0x7a, v82
	v_add_u32_e32 v83, 0x79, v83
	v_add_u32_e32 v84, 0x78, v84
	v_add_u32_e32 v85, 0x77, v85
	v_add_u32_e32 v86, 0x76, v86
	v_add_u32_e32 v87, 0x75, v87
	v_add_u32_e32 v88, 0x74, v88
	v_add_u32_e32 v89, 0x73, v89
	v_add_u32_e32 v90, 0x72, v90
	v_add_u32_e32 v91, 0x71, v91
	v_add_u32_e32 v92, 0x70, v92
	v_max_u32_e32 v93, v77, v78
	v_min_u32_e32 v77, v77, v78
	v_max_u32_e32 v78, v80, v79
	v_min_u32_e32 v79, v80, v79
	v_max_u32_e32 v80, v81, v82
	v_min_u32_e32 v81, v81, v82
	v_max_u32_e32 v82, v84, v83
	v_min_u32_e32 v83, v84, v83
	v_max_u32_e32 v84, v85, v86
	v_min_u32_e32 v85, v85, v86
	v_max_u32_e32 v86, v88, v87
	v_min_u32_e32 v87, v88, v87
	v_max_u32_e32 v88, v89, v90
	v_min_u32_e32 v89, v89, v90
	v_max_u32_e32 v90, v92, v91
	v_min_u32_e32 v91, v92, v91
	v_max_u32_e32 v92, v93, v79
	v_min_u32_e32 v79, v93, v79
	v_max_u32_e32 v93, v77, v78
	v_min_u32_e32 v77, v77, v78
	v_max_u32_e32 v78, v83, v80
	v_min_u32_e32 v80, v83, v80
	v_max_u32_e32 v83, v82, v81
	v_min_u32_e32 v81, v82, v81
	v_max_u32_e32 v82, v84, v87
	v_min_u32_e32 v84, v84, v87
	v_max_u32_e32 v87, v85, v86
	v_min_u32_e32 v85, v85, v86
	v_max_u32_e32 v86, v91, v88
	v_min_u32_e32 v88, v91, v88
	v_max_u32_e32 v91, v90, v89
	v_min_u32_e32 v89, v90, v89
	v_max_u32_e32 v90, v92, v93
	v_min_u32_e32 v92, v92, v93
	v_max_u32_e32 v93, v79, v77
	v_min_u32_e32 v77, v79, v77
	v_max_u32_e32 v79, v81, v80
	v_min_u32_e32 v80, v81, v80
	v_max_u32_e32 v81, v83, v78
	v_min_u32_e32 v78, v83, v78
	v_max_u32_e32 v83, v82, v87
	v_min_u32_e32 v82, v82, v87
	v_max_u32_e32 v87, v84, v85
	v_min_u32_e32 v84, v84, v85
	v_max_u32_e32 v85, v89, v88
	v_min_u32_e32 v88, v89, v88
	v_max_u32_e32 v89, v91, v86
	v_min_u32_e32 v86, v91, v86
	v_max_u32_e32 v91, v90, v80
	v_min_u32_e32 v80, v90, v80
	v_max_u32_e32 v90, v92, v79
	v_min_u32_e32 v79, v92, v79
	v_max_u32_e32 v92, v93, v78
; #define CE_DESC(x, y) do { const unsigned mx_ = (x) > (y) ? (x) : (y); const unsigned mn_ = (x) > (y) ? (y) : (x); (x) = mx_; (y) = mn_; } while (0)
; DI void sort16_desc(unsigned (&a)[16]) {
; #pragma unroll
;   for (int k = 2; k <= 16; k <<= 1)
; #pragma unroll
;     for (int j = k >> 1; j > 0; j >>= 1)
; #pragma unroll
;       for (int i = 0; i < 16; ++i) {
;         const int l = i ^ j;
;         if (l > i) { if ((i & k) == 0) CE_DESC(a[i], a[l]); else CE_DESC(a[l], a[i]); }
;       }
; }
; DI void merge16_desc(unsigned (&a)[16], const unsigned (&b)[16]) {
; #pragma unroll
;   for (int i = 0; i < 16; ++i) a[i] = a[i] > b[15 - i] ? a[i] : b[15 - i];
; #pragma unroll
;   for (int j = 8; j > 0; j >>= 1)
; #pragma unroll
;     for (int i = 0; i < 16; ++i) if ((i & j) == 0) CE_DESC(a[i], a[i + j]);
; }
; DI void peer_select_unit(const Params& p, int unit, char* lds, const bf16x8 (&kb)[4][4]) {
;     ...
;     dpp16<0xB1>(bq, a); merge16_desc(a, bq);
;     dpp16<0x4E>(bq, a); merge16_desc(a, bq);
	v_min_u32_e32 v78, v93, v78
	v_max_u32_e32 v93, v77, v81
	v_min_u32_e32 v77, v77, v81
	v_max_u32_e32 v81, v88, v83
	v_min_u32_e32 v83, v88, v83
	v_max_u32_e32 v88, v85, v82
	v_min_u32_e32 v82, v85, v82
	v_max_u32_e32 v85, v86, v87
	v_min_u32_e32 v86, v86, v87
	v_max_u32_e32 v87, v89, v84
	v_min_u32_e32 v84, v89, v84
	v_max_u32_e32 v89, v91, v92
	v_min_u32_e32 v91, v91, v92
	v_max_u32_e32 v92, v90, v93
	v_min_u32_e32 v90, v90, v93
	v_max_u32_e32 v93, v80, v78
	v_min_u32_e32 v78, v80, v78
	v_max_u32_e32 v80, v79, v77
	v_min_u32_e32 v77, v79, v77
	v_max_u32_e32 v79, v86, v83
	v_min_u32_e32 v83, v86, v83
	v_max_u32_e32 v86, v84, v82
	v_min_u32_e32 v82, v84, v82
	v_max_u32_e32 v84, v85, v81
	v_min_u32_e32 v81, v85, v81
	v_max_u32_e32 v85, v87, v88
	v_min_u32_e32 v87, v87, v88
	v_max_u32_e32 v88, v89, v92
	v_min_u32_e32 v89, v89, v92
	v_max_u32_e32 v92, v91, v90
	v_min_u32_e32 v90, v91, v90
	v_max_u32_e32 v91, v93, v80
	v_min_u32_e32 v80, v93, v80
	v_max_u32_e32 v93, v78, v77
	v_min_u32_e32 v77, v78, v77
	v_max_u32_e32 v78, v82, v83
	v_min_u32_e32 v82, v82, v83
	v_max_u32_e32 v83, v86, v79
	v_min_u32_e32 v79, v86, v79
	v_max_u32_e32 v86, v87, v81
	v_min_u32_e32 v81, v87, v81
	v_max_u32_e32 v87, v85, v84
	v_min_u32_e32 v84, v85, v84
	v_max_u32_e32 v85, v88, v82
	v_min_u32_e32 v82, v88, v82
	v_max_u32_e32 v88, v89, v78
	v_min_u32_e32 v78, v89, v78
	v_max_u32_e32 v89, v92, v79
	v_min_u32_e32 v79, v92, v79
	v_max_u32_e32 v92, v90, v83
	v_min_u32_e32 v83, v90, v83
	v_max_u32_e32 v90, v91, v81
	v_min_u32_e32 v81, v91, v81
	v_max_u32_e32 v91, v80, v86
	v_min_u32_e32 v80, v80, v86
	v_max_u32_e32 v86, v93, v84
	v_min_u32_e32 v84, v93, v84
	v_max_u32_e32 v93, v77, v87
	v_min_u32_e32 v77, v77, v87
	v_max_u32_e32 v87, v85, v90
	v_min_u32_e32 v85, v85, v90
	v_max_u32_e32 v90, v88, v91
	v_min_u32_e32 v88, v88, v91
	v_max_u32_e32 v91, v89, v86
	v_min_u32_e32 v86, v89, v86
	v_max_u32_e32 v89, v92, v93
	v_min_u32_e32 v92, v92, v93
	v_max_u32_e32 v93, v82, v81
	v_min_u32_e32 v81, v82, v81
	v_max_u32_e32 v82, v78, v80
	v_min_u32_e32 v78, v78, v80
	v_max_u32_e32 v80, v79, v84
	v_min_u32_e32 v79, v79, v84
	v_max_u32_e32 v84, v83, v77
	v_min_u32_e32 v77, v83, v77
	v_max_u32_e32 v83, v87, v91
	v_min_u32_e32 v87, v87, v91
	v_max_u32_e32 v91, v90, v89
	v_min_u32_e32 v89, v90, v89
	v_max_u32_e32 v90, v85, v86
	v_min_u32_e32 v85, v85, v86
	v_max_u32_e32 v86, v88, v92
	v_min_u32_e32 v88, v88, v92
	v_max_u32_e32 v92, v93, v80
	v_min_u32_e32 v80, v93, v80
	v_max_u32_e32 v93, v82, v84
	v_min_u32_e32 v82, v82, v84
	v_max_u32_e32 v84, v81, v79
	v_min_u32_e32 v79, v81, v79
	v_max_u32_e32 v81, v78, v77
	v_min_u32_e32 v77, v78, v77
	v_max_u32_e32 v78, v83, v91
	v_min_u32_e32 v83, v83, v91
	v_max_u32_e32 v91, v87, v89
	v_min_u32_e32 v87, v87, v89
	v_max_u32_e32 v89, v90, v86
	v_min_u32_e32 v86, v90, v86
	v_max_u32_e32 v90, v85, v88
	v_min_u32_e32 v85, v85, v88
	v_max_u32_e32 v88, v92, v93
	v_min_u32_e32 v92, v92, v93
	v_max_u32_e32 v93, v80, v82
	v_min_u32_e32 v80, v80, v82
	v_max_u32_e32 v82, v84, v81
	v_min_u32_e32 v81, v84, v81
	v_max_u32_e32 v84, v79, v77
	v_min_u32_e32 v77, v79, v77
	v_mov_b32_dpp v79, v78 quad_perm:[1,0,3,2] row_mask:0xf bank_mask:0xf bound_ctrl:1
	v_mov_b32_dpp v94, v83 quad_perm:[1,0,3,2] row_mask:0xf bank_mask:0xf bound_ctrl:1
	v_mov_b32_dpp v95, v91 quad_perm:[1,0,3,2] row_mask:0xf bank_mask:0xf bound_ctrl:1
	v_mov_b32_dpp v96, v87 quad_perm:[1,0,3,2] row_mask:0xf bank_mask:0xf bound_ctrl:1
	v_mov_b32_dpp v97, v89 quad_perm:[1,0,3,2] row_mask:0xf bank_mask:0xf bound_ctrl:1
	v_mov_b32_dpp v98, v86 quad_perm:[1,0,3,2] row_mask:0xf bank_mask:0xf bound_ctrl:1
	v_max_u32_dpp v78, v77, v78 quad_perm:[1,0,3,2] row_mask:0xf bank_mask:0xf bound_ctrl:1
	v_max_u32_dpp v83, v84, v83 quad_perm:[1,0,3,2] row_mask:0xf bank_mask:0xf bound_ctrl:1
	v_max_u32_dpp v91, v81, v91 quad_perm:[1,0,3,2] row_mask:0xf bank_mask:0xf bound_ctrl:1
	v_max_u32_dpp v87, v82, v87 quad_perm:[1,0,3,2] row_mask:0xf bank_mask:0xf bound_ctrl:1
	v_max_u32_dpp v89, v80, v89 quad_perm:[1,0,3,2] row_mask:0xf bank_mask:0xf bound_ctrl:1
	v_max_u32_dpp v86, v93, v86 quad_perm:[1,0,3,2] row_mask:0xf bank_mask:0xf bound_ctrl:1
	v_max_u32_dpp v99, v92, v90 quad_perm:[1,0,3,2] row_mask:0xf bank_mask:0xf bound_ctrl:1
	v_max_u32_dpp v100, v88, v85 quad_perm:[1,0,3,2] row_mask:0xf bank_mask:0xf bound_ctrl:1
	v_max_u32_dpp v85, v85, v88 quad_perm:[1,0,3,2] row_mask:0xf bank_mask:0xf bound_ctrl:1
	v_max_u32_dpp v88, v90, v92 quad_perm:[1,0,3,2] row_mask:0xf bank_mask:0xf bound_ctrl:1
	v_max_u32_e32 v90, v93, v98
	v_max_u32_e32 v80, v80, v97
	v_max_u32_e32 v82, v82, v96
	v_max_u32_e32 v81, v81, v95
	v_max_u32_e32 v84, v84, v94
	v_max_u32_e32 v77, v77, v79
	v_max_u32_e32 v79, v78, v85
	v_min_u32_e32 v78, v78, v85
	v_max_u32_e32 v85, v83, v88
	v_min_u32_e32 v83, v83, v88
	v_max_u32_e32 v88, v91, v90
	v_min_u32_e32 v90, v91, v90
	v_max_u32_e32 v91, v87, v80
	v_min_u32_e32 v80, v87, v80
	v_max_u32_e32 v87, v89, v82
	v_min_u32_e32 v82, v89, v82
	v_max_u32_e32 v89, v86, v81
	v_min_u32_e32 v81, v86, v81
	v_max_u32_e32 v86, v99, v84
	v_max_u32_e32 v92, v100, v77
	v_min_u32_e32 v84, v99, v84
	v_min_u32_e32 v77, v100, v77
	v_max_u32_e32 v93, v79, v87
	v_min_u32_e32 v79, v79, v87
	v_max_u32_e32 v87, v85, v89
	v_min_u32_e32 v85, v85, v89
	v_max_u32_e32 v89, v88, v86
	v_min_u32_e32 v86, v88, v86
	v_max_u32_e32 v88, v91, v92
	v_min_u32_e32 v91, v91, v92
	v_max_u32_e32 v92, v78, v82
	v_min_u32_e32 v78, v78, v82
	v_max_u32_e32 v82, v83, v81
	v_min_u32_e32 v81, v83, v81
	v_max_u32_e32 v83, v90, v84
	v_min_u32_e32 v84, v90, v84
	v_max_u32_e32 v90, v80, v77
	v_min_u32_e32 v77, v80, v77
	v_max_u32_e32 v80, v93, v89
; #define CE_DESC(x, y) do { const unsigned mx_ = (x) > (y) ? (x) : (y); const unsigned mn_ = (x) > (y) ? (y) : (x); (x) = mx_; (y) = mn_; } while (0)
; DI void merge16_desc(unsigned (&a)[16], const unsigned (&b)[16]) {
; #pragma unroll
;   for (int i = 0; i < 16; ++i) a[i] = a[i] > b[15 - i] ? a[i] : b[15 - i];
; #pragma unroll
;   for (int j = 8; j > 0; j >>= 1)
; #pragma unroll
;     for (int i = 0; i < 16; ++i) if ((i & j) == 0) CE_DESC(a[i], a[i + j]);
; }
; DI void peer_select_unit(const Params& p, int unit, char* lds, const bf16x8 (&kb)[4][4]) {
;     ...
;     dpp16<0x4E>(bq, a); merge16_desc(a, bq);
;     dpp16<0x141>(bq, a); merge16_desc(a, bq);
	v_min_u32_e32 v89, v93, v89
	v_max_u32_e32 v93, v87, v88
	v_min_u32_e32 v87, v87, v88
	v_max_u32_e32 v88, v79, v86
	v_min_u32_e32 v79, v79, v86
	v_max_u32_e32 v86, v85, v91
	v_min_u32_e32 v85, v85, v91
	v_max_u32_e32 v91, v92, v83
	v_min_u32_e32 v83, v92, v83
	v_max_u32_e32 v92, v82, v90
	v_min_u32_e32 v82, v82, v90
	v_max_u32_e32 v90, v78, v84
	v_min_u32_e32 v78, v78, v84
	v_max_u32_e32 v84, v81, v77
	v_min_u32_e32 v77, v81, v77
	v_max_u32_e32 v81, v80, v93
	v_min_u32_e32 v80, v80, v93
	v_max_u32_e32 v93, v89, v87
	v_min_u32_e32 v87, v89, v87
	v_max_u32_e32 v89, v88, v86
	v_min_u32_e32 v86, v88, v86
	v_max_u32_e32 v88, v79, v85
	v_min_u32_e32 v79, v79, v85
	v_max_u32_e32 v85, v91, v92
	v_min_u32_e32 v91, v91, v92
	v_max_u32_e32 v92, v83, v82
	v_min_u32_e32 v82, v83, v82
	v_max_u32_e32 v83, v90, v84
	v_min_u32_e32 v84, v90, v84
	v_max_u32_e32 v90, v78, v77
	v_min_u32_e32 v77, v78, v77
	v_mov_b32_dpp v78, v81 quad_perm:[2,3,0,1] row_mask:0xf bank_mask:0xf bound_ctrl:1
	v_mov_b32_dpp v94, v80 quad_perm:[2,3,0,1] row_mask:0xf bank_mask:0xf bound_ctrl:1
	v_mov_b32_dpp v95, v93 quad_perm:[2,3,0,1] row_mask:0xf bank_mask:0xf bound_ctrl:1
	v_mov_b32_dpp v96, v87 quad_perm:[2,3,0,1] row_mask:0xf bank_mask:0xf bound_ctrl:1
	v_mov_b32_dpp v97, v89 quad_perm:[2,3,0,1] row_mask:0xf bank_mask:0xf bound_ctrl:1
	v_mov_b32_dpp v98, v86 quad_perm:[2,3,0,1] row_mask:0xf bank_mask:0xf bound_ctrl:1
	v_max_u32_dpp v81, v77, v81 quad_perm:[2,3,0,1] row_mask:0xf bank_mask:0xf bound_ctrl:1
	v_max_u32_dpp v80, v90, v80 quad_perm:[2,3,0,1] row_mask:0xf bank_mask:0xf bound_ctrl:1
	v_max_u32_dpp v93, v84, v93 quad_perm:[2,3,0,1] row_mask:0xf bank_mask:0xf bound_ctrl:1
	v_max_u32_dpp v87, v83, v87 quad_perm:[2,3,0,1] row_mask:0xf bank_mask:0xf bound_ctrl:1
	v_max_u32_dpp v89, v82, v89 quad_perm:[2,3,0,1] row_mask:0xf bank_mask:0xf bound_ctrl:1
	v_max_u32_dpp v86, v92, v86 quad_perm:[2,3,0,1] row_mask:0xf bank_mask:0xf bound_ctrl:1
	v_max_u32_dpp v99, v91, v88 quad_perm:[2,3,0,1] row_mask:0xf bank_mask:0xf bound_ctrl:1
	v_max_u32_dpp v100, v85, v79 quad_perm:[2,3,0,1] row_mask:0xf bank_mask:0xf bound_ctrl:1
	v_max_u32_dpp v79, v79, v85 quad_perm:[2,3,0,1] row_mask:0xf bank_mask:0xf bound_ctrl:1
	v_max_u32_dpp v85, v88, v91 quad_perm:[2,3,0,1] row_mask:0xf bank_mask:0xf bound_ctrl:1
	v_max_u32_e32 v88, v92, v98
	v_max_u32_e32 v82, v82, v97
	v_max_u32_e32 v83, v83, v96
	v_max_u32_e32 v84, v84, v95
	v_max_u32_e32 v90, v90, v94
	v_max_u32_e32 v77, v77, v78
	v_max_u32_e32 v78, v81, v79
	v_min_u32_e32 v79, v81, v79
	v_max_u32_e32 v81, v80, v85
	v_min_u32_e32 v80, v80, v85
	v_max_u32_e32 v85, v93, v88
	v_max_u32_e32 v91, v87, v82
	v_min_u32_e32 v82, v87, v82
	v_max_u32_e32 v87, v89, v83
	v_min_u32_e32 v83, v89, v83
	v_max_u32_e32 v89, v86, v84
	v_min_u32_e32 v84, v86, v84
	v_max_u32_e32 v86, v99, v90
	v_max_u32_e32 v92, v100, v77
	v_min_u32_e32 v88, v93, v88
	v_min_u32_e32 v90, v99, v90
	v_min_u32_e32 v77, v100, v77
	v_max_u32_e32 v93, v78, v87
	v_min_u32_e32 v78, v78, v87
	v_max_u32_e32 v87, v81, v89
	v_min_u32_e32 v81, v81, v89
	v_max_u32_e32 v89, v85, v86
	v_min_u32_e32 v85, v85, v86
	v_max_u32_e32 v86, v91, v92
	v_min_u32_e32 v91, v91, v92
	v_max_u32_e32 v92, v79, v83
	v_min_u32_e32 v79, v79, v83
	v_max_u32_e32 v83, v80, v84
	v_min_u32_e32 v80, v80, v84
	v_max_u32_e32 v84, v88, v90
	v_min_u32_e32 v88, v88, v90
	v_max_u32_e32 v90, v82, v77
	v_min_u32_e32 v77, v82, v77
	v_max_u32_e32 v82, v93, v89
	v_min_u32_e32 v89, v93, v89
	v_max_u32_e32 v93, v87, v86
	v_min_u32_e32 v86, v87, v86
	v_max_u32_e32 v87, v78, v85
	v_min_u32_e32 v78, v78, v85
	v_max_u32_e32 v85, v81, v91
	v_min_u32_e32 v81, v81, v91
	v_max_u32_e32 v91, v92, v84
	v_min_u32_e32 v84, v92, v84
	v_max_u32_e32 v92, v83, v90
	v_min_u32_e32 v83, v83, v90
	v_max_u32_e32 v90, v79, v88
	v_min_u32_e32 v79, v79, v88
	v_max_u32_e32 v88, v80, v77
	v_min_u32_e32 v77, v80, v77
	v_max_u32_e32 v80, v82, v93
	v_min_u32_e32 v82, v82, v93
	v_max_u32_e32 v93, v89, v86
	v_min_u32_e32 v86, v89, v86
	v_max_u32_e32 v89, v87, v85
	v_min_u32_e32 v85, v87, v85
	v_max_u32_e32 v87, v78, v81
	v_min_u32_e32 v78, v78, v81
	v_max_u32_e32 v81, v91, v92
	v_min_u32_e32 v91, v91, v92
	v_max_u32_e32 v92, v84, v83
	v_min_u32_e32 v83, v84, v83
	v_max_u32_e32 v84, v90, v88
	v_min_u32_e32 v88, v90, v88
	v_max_u32_e32 v90, v79, v77
	v_min_u32_e32 v77, v79, v77
	v_mov_b32_dpp v79, v80 row_half_mirror row_mask:0xf bank_mask:0xf bound_ctrl:1
	v_mov_b32_dpp v94, v82 row_half_mirror row_mask:0xf bank_mask:0xf bound_ctrl:1
	v_mov_b32_dpp v95, v93 row_half_mirror row_mask:0xf bank_mask:0xf bound_ctrl:1
	v_mov_b32_dpp v96, v86 row_half_mirror row_mask:0xf bank_mask:0xf bound_ctrl:1
	v_mov_b32_dpp v97, v89 row_half_mirror row_mask:0xf bank_mask:0xf bound_ctrl:1
	v_mov_b32_dpp v98, v85 row_half_mirror row_mask:0xf bank_mask:0xf bound_ctrl:1
	v_max_u32_dpp v80, v77, v80 row_half_mirror row_mask:0xf bank_mask:0xf bound_ctrl:1
	v_max_u32_dpp v82, v90, v82 row_half_mirror row_mask:0xf bank_mask:0xf bound_ctrl:1
	v_max_u32_dpp v93, v88, v93 row_half_mirror row_mask:0xf bank_mask:0xf bound_ctrl:1
	v_max_u32_dpp v86, v84, v86 row_half_mirror row_mask:0xf bank_mask:0xf bound_ctrl:1
	v_max_u32_dpp v89, v83, v89 row_half_mirror row_mask:0xf bank_mask:0xf bound_ctrl:1
	v_max_u32_dpp v85, v92, v85 row_half_mirror row_mask:0xf bank_mask:0xf bound_ctrl:1
	v_max_u32_dpp v99, v91, v87 row_half_mirror row_mask:0xf bank_mask:0xf bound_ctrl:1
	v_max_u32_dpp v100, v81, v78 row_half_mirror row_mask:0xf bank_mask:0xf bound_ctrl:1
	v_max_u32_dpp v78, v78, v81 row_half_mirror row_mask:0xf bank_mask:0xf bound_ctrl:1
	v_max_u32_dpp v81, v87, v91 row_half_mirror row_mask:0xf bank_mask:0xf bound_ctrl:1
; DI unsigned ordkey(float f) { const unsigned u = __float_as_uint(f); return (u & 0x80000000u) ? ~u : (u | 0x80000000u); }
; DI void peer_select_unit(const Params& p, int unit, char* lds, const bf16x8 (&kb)[4][4]) {
;     ...
; #pragma unroll
;     for (int s = 0; s < 2; ++s) {
;       unsigned k = 0u;
; #pragma unroll
;       for (int q = 0; q < 8; ++q) k = part == q ? a[2 * q + s] : k;
;       const int idx = 127 - (int)(k & 127u);
;       topv[rr * 16 + 2 * part + s] = sc[rr * 132 + idx]; topi[rr * 16 + 2 * part + s] = idx;
;     }
;   }
;   __syncthreads();
;   if (tid < 128) {
;     const int tok = tid >> 2, q4 = tid & 3;
;     unsigned c[16], bq[16];
; #pragma unroll
;     for (int i = 0; i < 16; ++i) {
;       const unsigned code = PEER_CAND[16 * q4 + i];
;       const float v = topv[tok * 16 + ((code >> 4) & 15)] + topv[(32 + tok) * 16 + (code & 15)];
;       c[i] = code == 0xFFu ? 0u : ((ordkey(v) & ~255u) | (255u - code));
	v_max_u32_e32 v87, v92, v98
	v_max_u32_e32 v83, v83, v97
	v_max_u32_e32 v84, v84, v96
	v_max_u32_e32 v88, v88, v95
	v_max_u32_e32 v90, v90, v94
	v_max_u32_e32 v77, v77, v79
	v_max_u32_e32 v79, v80, v78
	v_min_u32_e32 v78, v80, v78
	v_max_u32_e32 v80, v82, v81
	v_min_u32_e32 v81, v82, v81
	v_max_u32_e32 v82, v93, v87
	v_max_u32_e32 v91, v86, v83
	v_min_u32_e32 v83, v86, v83
	v_max_u32_e32 v86, v89, v84
	v_min_u32_e32 v84, v89, v84
	v_max_u32_e32 v89, v85, v88
	v_min_u32_e32 v85, v85, v88
	v_max_u32_e32 v88, v99, v90
	v_max_u32_e32 v92, v100, v77
	v_min_u32_e32 v87, v93, v87
	v_min_u32_e32 v90, v99, v90
	v_min_u32_e32 v77, v100, v77
	v_max_u32_e32 v93, v79, v86
	v_min_u32_e32 v79, v79, v86
	v_max_u32_e32 v86, v80, v89
	v_min_u32_e32 v80, v80, v89
	v_max_u32_e32 v89, v82, v88
	v_min_u32_e32 v82, v82, v88
	v_max_u32_e32 v88, v91, v92
	v_min_u32_e32 v91, v91, v92
	v_max_u32_e32 v92, v78, v84
	v_min_u32_e32 v78, v78, v84
	v_max_u32_e32 v84, v81, v85
	v_min_u32_e32 v81, v81, v85
	v_max_u32_e32 v85, v87, v90
	v_min_u32_e32 v87, v87, v90
	v_max_u32_e32 v90, v83, v77
	v_min_u32_e32 v77, v83, v77
	v_max_u32_e32 v83, v93, v89
	v_min_u32_e32 v89, v93, v89
	v_max_u32_e32 v93, v86, v88
	v_min_u32_e32 v86, v86, v88
	v_max_u32_e32 v88, v79, v82
	v_min_u32_e32 v79, v79, v82
	v_max_u32_e32 v82, v80, v91
	v_min_u32_e32 v80, v80, v91
	v_max_u32_e32 v91, v92, v85
	v_min_u32_e32 v85, v92, v85
	v_max_u32_e32 v92, v84, v90
	v_min_u32_e32 v84, v84, v90
	v_max_u32_e32 v90, v78, v87
	v_min_u32_e32 v78, v78, v87
	v_max_u32_e32 v87, v81, v77
	v_min_u32_e32 v77, v81, v77
	v_max_u32_e32 v81, v83, v93
	v_min_u32_e32 v83, v83, v93
	v_max_u32_e32 v93, v89, v86
	v_min_u32_e32 v86, v89, v86
	v_max_u32_e32 v89, v88, v82
	v_min_u32_e32 v82, v88, v82
	v_max_u32_e32 v88, v79, v80
	v_min_u32_e32 v79, v79, v80
	v_max_u32_e32 v80, v91, v92
	v_min_u32_e32 v91, v91, v92
	v_max_u32_e32 v92, v85, v84
	v_min_u32_e32 v84, v85, v84
	v_max_u32_e32 v85, v90, v87
	v_min_u32_e32 v87, v90, v87
	v_max_u32_e32 v90, v78, v77
	v_min_u32_e32 v77, v78, v77
	v_cndmask_b32_e64 v78, 0, v81, s[0:1]
	v_cndmask_b32_e64 v78, v78, v93, s[4:5]
	v_cndmask_b32_e64 v78, v78, v89, s[6:7]
	v_cndmask_b32_e64 v78, v78, v88, s[8:9]
	v_cndmask_b32_e64 v78, v78, v80, s[10:11]
	v_cndmask_b32_e64 v78, v78, v92, s[12:13]
	v_cndmask_b32_e64 v81, 0, v83, s[0:1]
	v_cndmask_b32_e64 v78, v78, v85, s[14:15]
	v_cndmask_b32_e64 v81, v81, v86, s[4:5]
	v_cndmask_b32_e64 v78, v78, v90, s[16:17]
	v_cndmask_b32_e64 v81, v81, v82, s[6:7]
	v_bitop3_b32 v78, v78, s3, v78 bitop3:0xc
	v_cndmask_b32_e64 v79, v81, v79, s[8:9]
	v_lshlrev_b32_e32 v80, 2, v78
	v_cndmask_b32_e64 v79, v79, v91, s[10:11]
	v_add3_u32 v80, v146, v80, v76
	v_cndmask_b32_e64 v79, v79, v84, s[12:13]
	ds_read_b32 v80, v80
	v_cndmask_b32_e64 v79, v79, v87, s[14:15]
	v_cndmask_b32_e64 v77, v79, v77, s[16:17]
	v_lshl_or_b32 v71, v71, 6, v69
	v_bitop3_b32 v79, v77, s3, v77 bitop3:0xc
	v_add_u32_e32 v71, v146, v71
	v_lshlrev_b32_e32 v77, 2, v79
	v_add3_u32 v76, v146, v77, v76
	s_waitcnt lgkmcnt(0)
	ds_write_b32 v71, v80 offset:33792
	ds_read_b32 v76, v76
	v_cmp_ne_u32_e32 vcc, 1, v70
	s_mov_b32 s69, 32
	s_mov_b64 s[20:21], 0
	ds_write_b64 v71, v[78:79] offset:37888
	s_waitcnt lgkmcnt(1)
	ds_write_b32 v71, v76 offset:33796
	s_cbranch_vccz .LBB0_1653
	v_cmp_gt_i32_e32 vcc, s18, v66
	s_waitcnt lgkmcnt(0)
	s_barrier
	s_and_saveexec_b64 s[8:9], vcc
	s_cbranch_execz .LBB0_1651
	v_and_b32_e32 v77, 3, v66
	v_lshlrev_b32_e32 v64, 4, v77
	s_getpc_b64 s[0:1]
	s_add_u32 s0, s0, _ZL9PEER_CAND@rel32@lo+4
	s_addc_u32 s1, s1, _ZL9PEER_CAND@rel32@hi+12
	global_load_ushort v80, v64, s[0:1]
	global_load_dwordx4 v[190:193], v64, s[0:1]
	v_lshlrev_b32_e32 v66, 6, v75
	v_lshlrev_b32_e32 v76, 4, v75
	v_lshl_add_u64 v[70:71], s[0:1], 0, v[64:65]
	v_cmp_eq_u32_e32 vcc, 3, v77
	v_cmp_ne_u32_e64 s[0:1], 3, v77
	v_mov_b32_e32 v82, 0
	s_waitcnt vmcnt(0)
	v_lshrrev_b32_e32 v67, 2, v80
	v_and_b32_e32 v68, 15, v80
	v_lshrrev_b16_e32 v79, 8, v80
	v_and_b32_e32 v67, 60, v67
	v_lshlrev_b32_e32 v68, 2, v68
	v_lshrrev_b32_e32 v69, 2, v79
	v_and_b32_e32 v78, 15, v79
	v_add3_u32 v67, v146, v67, v66
	v_add3_u32 v68, v146, v68, v66
	v_and_b32_e32 v69, 60, v69
	v_lshlrev_b32_e32 v78, 2, v78
	v_add3_u32 v81, v146, v69, v66
	v_add3_u32 v78, v146, v78, v66
	ds_read_b32 v67, v67 offset:33792
	ds_read_b32 v69, v68 offset:35840
	ds_read_b32 v66, v81 offset:33792
	ds_read_b32 v68, v78 offset:35840
	v_mov_b32_e32 v81, 0
	v_lshlrev_b32_e32 v78, 2, v76
	s_and_saveexec_b64 s[6:7], s[0:1]
	s_cbranch_execz .LBB0_1657
	v_bfe_u32 v82, v190, 16, 8
	v_lshrrev_b32_e32 v83, 2, v82
	v_and_b32_e32 v84, 15, v82
	v_and_b32_e32 v83, 60, v83
	v_lshlrev_b32_e32 v84, 2, v84
	v_add3_u32 v83, v146, v83, v78
	v_add3_u32 v84, v146, v84, v78
	ds_read_b32 v83, v83 offset:33792
	ds_read_b32 v84, v84 offset:35840
	s_waitcnt lgkmcnt(0)
	v_add_f32_e32 v83, v83, v84
	v_not_b32_e32 v84, v83
	v_or_b32_e32 v85, 0x80000000, v83
	v_cmp_gt_i32_e64 s[4:5], 0, v83
	s_nop 1
	v_cndmask_b32_e64 v83, v85, v84, s[4:5]
	v_and_b32_e32 v83, 0xffffff00, v83
	v_bitop3_b32 v82, v83, s19, v82 bitop3:0x36
.LBB0_1657:
	s_or_b64 exec, exec, s[6:7]
	s_and_saveexec_b64 s[6:7], s[0:1]
	s_cbranch_execz .LBB0_1659
	v_bfe_u32 v81, v190, 24, 8
	v_lshrrev_b32_e32 v83, 2, v81
	v_and_b32_e32 v84, 15, v81
	v_and_b32_e32 v83, 60, v83
	v_lshlrev_b32_e32 v84, 2, v84
	v_add3_u32 v83, v146, v83, v78
	v_add3_u32 v84, v146, v84, v78
	ds_read_b32 v83, v83 offset:33792
	ds_read_b32 v84, v84 offset:35840
	s_waitcnt lgkmcnt(0)
	v_add_f32_e32 v83, v83, v84
	v_not_b32_e32 v84, v83
	v_or_b32_e32 v85, 0x80000000, v83
	v_cmp_gt_i32_e64 s[4:5], 0, v83
	s_nop 1
	v_cndmask_b32_e64 v83, v85, v84, s[4:5]
	v_and_b32_e32 v83, 0xffffff00, v83
	v_bitop3_b32 v81, v83, s19, v81 bitop3:0x36
; DI unsigned ordkey(float f) { const unsigned u = __float_as_uint(f); return (u & 0x80000000u) ? ~u : (u | 0x80000000u); }
; DI void peer_select_unit(const Params& p, int unit, char* lds, const bf16x8 (&kb)[4][4]) {
;     ...
; #pragma unroll
;     for (int i = 0; i < 16; ++i) {
;       const unsigned code = PEER_CAND[16 * q4 + i];
;       const float v = topv[tok * 16 + ((code >> 4) & 15)] + topv[(32 + tok) * 16 + (code & 15)];
;       c[i] = code == 0xFFu ? 0u : ((ordkey(v) & ~255u) | (255u - code));
.LBB0_1659:
	s_or_b64 exec, exec, s[6:7]
	v_mov_b32_e32 v83, 0
	v_mov_b32_e32 v84, 0
	s_and_saveexec_b64 s[6:7], s[0:1]
	s_cbranch_execz .LBB0_1661
	v_bfe_u32 v84, v191, 0, 8
	v_lshrrev_b32_e32 v85, 2, v84
	v_and_b32_e32 v86, 15, v84
	v_and_b32_e32 v85, 60, v85
	v_lshlrev_b32_e32 v86, 2, v86
	v_add3_u32 v85, v146, v85, v78
	v_add3_u32 v86, v146, v86, v78
	ds_read_b32 v85, v85 offset:33792
	ds_read_b32 v86, v86 offset:35840
	s_waitcnt lgkmcnt(0)
	v_add_f32_e32 v85, v85, v86
	v_not_b32_e32 v86, v85
	v_or_b32_e32 v87, 0x80000000, v85
	v_cmp_gt_i32_e64 s[4:5], 0, v85
	s_nop 1
	v_cndmask_b32_e64 v85, v87, v86, s[4:5]
	v_and_b32_e32 v85, 0xffffff00, v85
	v_bitop3_b32 v84, v85, s19, v84 bitop3:0x36
.LBB0_1661:
	s_or_b64 exec, exec, s[6:7]
	s_and_saveexec_b64 s[6:7], s[0:1]
	s_cbranch_execz .LBB0_1663
	v_bfe_u32 v83, v191, 8, 8
	v_lshrrev_b32_e32 v85, 2, v83
	v_and_b32_e32 v86, 15, v83
	v_and_b32_e32 v85, 60, v85
	v_lshlrev_b32_e32 v86, 2, v86
	v_add3_u32 v85, v146, v85, v78
	v_add3_u32 v86, v146, v86, v78
	ds_read_b32 v85, v85 offset:33792
	ds_read_b32 v86, v86 offset:35840
	s_waitcnt lgkmcnt(0)
	v_add_f32_e32 v85, v85, v86
	v_not_b32_e32 v86, v85
	v_or_b32_e32 v87, 0x80000000, v85
	v_cmp_gt_i32_e64 s[4:5], 0, v85
	s_nop 1
	v_cndmask_b32_e64 v85, v87, v86, s[4:5]
	v_and_b32_e32 v85, 0xffffff00, v85
	v_bitop3_b32 v83, v85, s19, v83 bitop3:0x36
.LBB0_1663:
	s_or_b64 exec, exec, s[6:7]
	v_mov_b32_e32 v85, 0
	v_mov_b32_e32 v86, 0
	s_and_saveexec_b64 s[6:7], s[0:1]
	s_cbranch_execz .LBB0_1665
	v_bfe_u32 v86, v191, 16, 8
	v_lshrrev_b32_e32 v87, 2, v86
	v_and_b32_e32 v88, 15, v86
	v_and_b32_e32 v87, 60, v87
	v_lshlrev_b32_e32 v88, 2, v88
	v_add3_u32 v87, v146, v87, v78
	v_add3_u32 v88, v146, v88, v78
	ds_read_b32 v87, v87 offset:33792
	ds_read_b32 v88, v88 offset:35840
	s_waitcnt lgkmcnt(0)
	v_add_f32_e32 v87, v87, v88
	v_not_b32_e32 v88, v87
	v_or_b32_e32 v89, 0x80000000, v87
	v_cmp_gt_i32_e64 s[4:5], 0, v87
	s_nop 1
	v_cndmask_b32_e64 v87, v89, v88, s[4:5]
	v_and_b32_e32 v87, 0xffffff00, v87
	v_bitop3_b32 v86, v87, s19, v86 bitop3:0x36
.LBB0_1665:
	s_or_b64 exec, exec, s[6:7]
	s_and_saveexec_b64 s[6:7], s[0:1]
	s_cbranch_execz .LBB0_1667
	v_bfe_u32 v85, v191, 24, 8
	v_lshrrev_b32_e32 v87, 2, v85
	v_and_b32_e32 v88, 15, v85
	v_and_b32_e32 v87, 60, v87
	v_lshlrev_b32_e32 v88, 2, v88
	v_add3_u32 v87, v146, v87, v78
	v_add3_u32 v88, v146, v88, v78
	ds_read_b32 v87, v87 offset:33792
	ds_read_b32 v88, v88 offset:35840
	s_waitcnt lgkmcnt(0)
	v_add_f32_e32 v87, v87, v88
	v_not_b32_e32 v88, v87
	v_or_b32_e32 v89, 0x80000000, v87
	v_cmp_gt_i32_e64 s[4:5], 0, v87
	s_nop 1
	v_cndmask_b32_e64 v87, v89, v88, s[4:5]
	v_and_b32_e32 v87, 0xffffff00, v87
	v_bitop3_b32 v85, v87, s19, v85 bitop3:0x36
.LBB0_1667:
	s_or_b64 exec, exec, s[6:7]
	v_mov_b32_e32 v87, 0
	v_mov_b32_e32 v88, 0
	s_and_saveexec_b64 s[6:7], s[0:1]
	s_cbranch_execz .LBB0_1669
	v_bfe_u32 v88, v192, 0, 8
	v_lshrrev_b32_e32 v89, 2, v88
	v_and_b32_e32 v90, 15, v88
	v_and_b32_e32 v89, 60, v89
	v_lshlrev_b32_e32 v90, 2, v90
	v_add3_u32 v89, v146, v89, v78
	v_add3_u32 v90, v146, v90, v78
	ds_read_b32 v89, v89 offset:33792
	ds_read_b32 v90, v90 offset:35840
	s_waitcnt lgkmcnt(0)
	v_add_f32_e32 v89, v89, v90
	v_not_b32_e32 v90, v89
	v_or_b32_e32 v91, 0x80000000, v89
	v_cmp_gt_i32_e64 s[4:5], 0, v89
	s_nop 1
	v_cndmask_b32_e64 v89, v91, v90, s[4:5]
	v_and_b32_e32 v89, 0xffffff00, v89
	v_bitop3_b32 v88, v89, s19, v88 bitop3:0x36
.LBB0_1669:
	s_or_b64 exec, exec, s[6:7]
	s_and_saveexec_b64 s[6:7], s[0:1]
	s_cbranch_execz .LBB0_1671
	v_bfe_u32 v87, v192, 8, 8
	v_lshrrev_b32_e32 v89, 2, v87
	v_and_b32_e32 v90, 15, v87
	v_and_b32_e32 v89, 60, v89
	v_lshlrev_b32_e32 v90, 2, v90
	v_add3_u32 v89, v146, v89, v78
	v_add3_u32 v90, v146, v90, v78
	ds_read_b32 v89, v89 offset:33792
	ds_read_b32 v90, v90 offset:35840
	s_waitcnt lgkmcnt(0)
	v_add_f32_e32 v89, v89, v90
	v_not_b32_e32 v90, v89
	v_or_b32_e32 v91, 0x80000000, v89
	v_cmp_gt_i32_e64 s[4:5], 0, v89
	s_nop 1
	v_cndmask_b32_e64 v89, v91, v90, s[4:5]
	v_and_b32_e32 v89, 0xffffff00, v89
	v_bitop3_b32 v87, v89, s19, v87 bitop3:0x36
; DI unsigned ordkey(float f) { const unsigned u = __float_as_uint(f); return (u & 0x80000000u) ? ~u : (u | 0x80000000u); }
; DI void peer_select_unit(const Params& p, int unit, char* lds, const bf16x8 (&kb)[4][4]) {
;     ...
; #pragma unroll
;     for (int i = 0; i < 16; ++i) {
;       const unsigned code = PEER_CAND[16 * q4 + i];
;       const float v = topv[tok * 16 + ((code >> 4) & 15)] + topv[(32 + tok) * 16 + (code & 15)];
;       c[i] = code == 0xFFu ? 0u : ((ordkey(v) & ~255u) | (255u - code));
.LBB0_1671:
	s_or_b64 exec, exec, s[6:7]
	v_mov_b32_e32 v89, 0
	v_mov_b32_e32 v90, 0
	s_and_saveexec_b64 s[6:7], s[0:1]
	s_cbranch_execz .LBB0_1673
	v_bfe_u32 v90, v192, 16, 8
	v_lshrrev_b32_e32 v91, 2, v90
	v_and_b32_e32 v92, 15, v90
	v_and_b32_e32 v91, 60, v91
	v_lshlrev_b32_e32 v92, 2, v92
	v_add3_u32 v91, v146, v91, v78
	v_add3_u32 v92, v146, v92, v78
	ds_read_b32 v91, v91 offset:33792
	ds_read_b32 v92, v92 offset:35840
	s_waitcnt lgkmcnt(0)
	v_add_f32_e32 v91, v91, v92
	v_not_b32_e32 v92, v91
	v_or_b32_e32 v93, 0x80000000, v91
	v_cmp_gt_i32_e64 s[4:5], 0, v91
	s_nop 1
	v_cndmask_b32_e64 v91, v93, v92, s[4:5]
	v_and_b32_e32 v91, 0xffffff00, v91
	v_bitop3_b32 v90, v91, s19, v90 bitop3:0x36
.LBB0_1673:
	s_or_b64 exec, exec, s[6:7]
	s_and_saveexec_b64 s[6:7], s[0:1]
	s_cbranch_execz .LBB0_1675
	v_bfe_u32 v89, v192, 24, 8
	v_lshrrev_b32_e32 v91, 2, v89
	v_and_b32_e32 v92, 15, v89
	v_and_b32_e32 v91, 60, v91
	v_lshlrev_b32_e32 v92, 2, v92
	v_add3_u32 v91, v146, v91, v78
	v_add3_u32 v92, v146, v92, v78
	ds_read_b32 v91, v91 offset:33792
	ds_read_b32 v92, v92 offset:35840
	s_waitcnt lgkmcnt(0)
	v_add_f32_e32 v91, v91, v92
	v_not_b32_e32 v92, v91
	v_or_b32_e32 v93, 0x80000000, v91
	v_cmp_gt_i32_e64 s[4:5], 0, v91
	s_nop 1
	v_cndmask_b32_e64 v91, v93, v92, s[4:5]
	v_and_b32_e32 v91, 0xffffff00, v91
	v_bitop3_b32 v89, v91, s19, v89 bitop3:0x36
.LBB0_1675:
	s_or_b64 exec, exec, s[6:7]
	v_mov_b32_e32 v91, 0
	v_mov_b32_e32 v92, 0
	s_and_saveexec_b64 s[6:7], s[0:1]
	s_cbranch_execz .LBB0_1677
	v_bfe_u32 v92, v193, 0, 8
	v_lshrrev_b32_e32 v93, 2, v92
	v_and_b32_e32 v94, 15, v92
	v_and_b32_e32 v93, 60, v93
	v_lshlrev_b32_e32 v94, 2, v94
	v_add3_u32 v93, v146, v93, v78
	v_add3_u32 v94, v146, v94, v78
	ds_read_b32 v93, v93 offset:33792
	ds_read_b32 v94, v94 offset:35840
	s_waitcnt lgkmcnt(0)
	v_add_f32_e32 v93, v93, v94
	v_not_b32_e32 v94, v93
	v_or_b32_e32 v95, 0x80000000, v93
	v_cmp_gt_i32_e64 s[4:5], 0, v93
	s_nop 1
	v_cndmask_b32_e64 v93, v95, v94, s[4:5]
	v_and_b32_e32 v93, 0xffffff00, v93
	v_bitop3_b32 v92, v93, s19, v92 bitop3:0x36
.LBB0_1677:
	s_or_b64 exec, exec, s[6:7]
	s_and_saveexec_b64 s[6:7], s[0:1]
	s_cbranch_execz .LBB0_1679
	v_bfe_u32 v91, v193, 8, 8
	v_lshrrev_b32_e32 v93, 2, v91
	v_and_b32_e32 v94, 15, v91
	v_and_b32_e32 v93, 60, v93
	v_lshlrev_b32_e32 v94, 2, v94
	v_add3_u32 v93, v146, v93, v78
	v_add3_u32 v94, v146, v94, v78
	ds_read_b32 v93, v93 offset:33792
	ds_read_b32 v94, v94 offset:35840
	s_waitcnt lgkmcnt(0)
	v_add_f32_e32 v93, v93, v94
	v_not_b32_e32 v94, v93
	v_or_b32_e32 v95, 0x80000000, v93
	v_cmp_gt_i32_e64 s[4:5], 0, v93
	s_nop 1
	v_cndmask_b32_e64 v93, v95, v94, s[4:5]
	v_and_b32_e32 v93, 0xffffff00, v93
	v_bitop3_b32 v91, v93, s19, v91 bitop3:0x36
.LBB0_1679:
	s_or_b64 exec, exec, s[6:7]
	v_mov_b32_e32 v93, 0
	v_mov_b32_e32 v94, 0
	s_and_saveexec_b64 s[6:7], s[0:1]
	s_cbranch_execz .LBB0_1681
	v_bfe_u32 v94, v193, 16, 8
	v_lshrrev_b32_e32 v95, 2, v94
	v_and_b32_e32 v96, 15, v94
	v_and_b32_e32 v95, 60, v95
	v_lshlrev_b32_e32 v96, 2, v96
	v_add3_u32 v95, v146, v95, v78
	v_add3_u32 v96, v146, v96, v78
	ds_read_b32 v95, v95 offset:33792
	ds_read_b32 v96, v96 offset:35840
	s_waitcnt lgkmcnt(0)
	v_add_f32_e32 v95, v95, v96
	v_not_b32_e32 v96, v95
	v_or_b32_e32 v97, 0x80000000, v95
	v_cmp_gt_i32_e64 s[4:5], 0, v95
	s_nop 1
	v_cndmask_b32_e64 v95, v97, v96, s[4:5]
	v_and_b32_e32 v95, 0xffffff00, v95
	v_bitop3_b32 v94, v95, s19, v94 bitop3:0x36
.LBB0_1681:
	s_or_b64 exec, exec, s[6:7]
	s_and_saveexec_b64 s[4:5], s[0:1]
	s_cbranch_execz .LBB0_1650
	v_bfe_u32 v70, v193, 24, 8
	v_lshrrev_b32_e32 v71, 2, v70
	v_and_b32_e32 v93, 15, v70
	v_and_b32_e32 v71, 60, v71
	v_lshlrev_b32_e32 v93, 2, v93
	v_add3_u32 v71, v146, v71, v78
	v_add3_u32 v93, v146, v93, v78
	ds_read_b32 v71, v71 offset:33792
	ds_read_b32 v93, v93 offset:35840
	s_waitcnt lgkmcnt(0)
	v_add_f32_e32 v71, v71, v93
	v_not_b32_e32 v93, v71
	v_or_b32_e32 v95, 0x80000000, v71
	v_cmp_gt_i32_e64 s[0:1], 0, v71
	s_nop 1
	v_cndmask_b32_e64 v71, v95, v93, s[0:1]
	v_and_b32_e32 v71, 0xffffff00, v71
	v_bitop3_b32 v93, v71, s19, v70 bitop3:0x36
	s_branch .LBB0_1650
